# v63 + work-queue tail split from entry 32: entries 32..63 keep half of their weight-copy chunk, 32 extra copy-only entries per XCD (96 entries)
# speedup vs baseline: 1.0079x; 1.0025x over previous
.LBB6_896:
	s_or_b64 exec, exec, s[2:3]
	v_readlane_b32 s0, v254, 30
	s_waitcnt lgkmcnt(0)
	s_barrier
	v_mov_b32_e32 v2, s0
	ds_read_b32 v2, v2
	s_mov_b64 s[2:3], -1
	s_waitcnt lgkmcnt(0)
	s_barrier
	v_readfirstlane_b32 s0, v2
	s_cmp_gt_i32 s0, 0x5f
	s_cbranch_scc1 .LBB6_891
	s_cmp_gt_i32 s0, 47
	s_cbranch_scc0 .LBB6_899
	s_sub_i32 s1, s0, 48
	s_lshr_b32 s92, s1, 1
	s_mov_b64 s[2:3], 0

.LBB6_901:
	s_lshl_b32 s84, s0, 3
	s_or_b32 s1, s84, s59
	s_lshl_b32 s2, s1, 1
	s_add_i32 s3, s1, 0x100
	s_cmp_lt_u32 s1, 0x100
	s_cselect_b32 s2, s2, s3
	s_mul_i32 s2, s63, s2
	s_lshr_b32 s2, s2, 10
	s_and_b32 s90, s2, 0xffffffe0
	s_add_i32 s1, s1, 1
	s_lshl_b32 s2, s1, 1
	s_add_i32 s3, s1, 0x100
	s_cmp_lt_u32 s1, 0x100
	s_cselect_b32 s2, s2, s3
	s_mul_i32 s2, s63, s2
	s_lshr_b32 s2, s2, 10
	s_and_b32 s91, s2, 0xffffffe0
	s_bitcmp0_b32 s0, 0
	s_cselect_b64 s[22:23], -1, 0
	s_and_b64 vcc, exec, s[22:23]
	s_cbranch_vccnz .LBB6_1210
	v_readfirstlane_b32 s98, v0
	s_nop 0
	s_bitcmp1_b32 s98, 8
	s_cbranch_scc0 .Ldephase_a
	s_sleep 80
